# v10 (KMAX loads hoisted in unit prologue) plus a 4-byte s_nop before the hand-written attention loop so its byte offset is 0 mod 8 (code-placement test)
# baseline (speedup 1.0000x reference)
.LBB0_1138:
	v_mov_b32_e32 v224, 0
	s_mov_b32 s1, 0
	v_mov_b32_e32 v36, 0
	v_mov_b32_e32 v37, 0
	v_mov_b32_e32 v38, 0
	v_mov_b32_e32 v39, 0
	v_mov_b32_e32 v40, 0
	v_mov_b32_e32 v41, 0
	v_mov_b32_e32 v42, 0
	v_mov_b32_e32 v43, 0
	v_mov_b32_e32 v44, 0
	v_mov_b32_e32 v45, 0
	v_mov_b32_e32 v46, 0
	v_mov_b32_e32 v47, 0
	v_mov_b32_e32 v48, 0
	v_mov_b32_e32 v49, 0
	v_mov_b32_e32 v50, 0
	v_mov_b32_e32 v51, 0
	v_mov_b32_e32 v52, 0
	v_mov_b32_e32 v53, 0
	v_mov_b32_e32 v54, 0
	v_mov_b32_e32 v55, 0
	v_mov_b32_e32 v56, 0
	v_mov_b32_e32 v57, 0
	v_mov_b32_e32 v58, 0
	v_mov_b32_e32 v59, 0
	v_mov_b32_e32 v60, 0
	v_mov_b32_e32 v61, 0
	v_mov_b32_e32 v62, 0
	v_mov_b32_e32 v63, 0
	v_mov_b32_e32 v64, 0
	v_mov_b32_e32 v65, 0
	v_mov_b32_e32 v66, 0
	v_mov_b32_e32 v67, 0
	v_add_u32_e32 v178, v218, v217
	v_add_u32_e32 v230, 0x10000, v205
	v_add_u32_e32 v231, 0x10000, v178
	v_add_u32_e32 v232, 0x10000, v219
	v_add_u32_e32 v233, 0x10000, v220
	v_add_u32_e32 v234, 0x10000, v221
	v_add_u32_e32 v235, 0x10000, v222
	ds_read_b128 v[166:169], v205 offset:13312
	ds_read_b128 v[170:173], v205 offset:19968
	ds_read_b128 v[174:177], v205 offset:13344
	ds_read_b128 v[206:209], v205 offset:20000
	ds_read_b128 v[226:229], v205 offset:13376
	s_add_i32 s2, s23, s1
	s_add_i32 s3, s2, 2
	s_add_i32 s2, s2, 1
	s_cmp_ge_u32 s2, s34
	s_cselect_b32 s7, s34, 0
	s_sub_i32 s2, s2, s7
	s_cmp_ge_u32 s3, s34
	s_cselect_b32 s7, s34, 0
	s_sub_i32 s3, s3, s7
	s_cmp_ge_u32 s3, s34
	s_cselect_b32 s7, s34, 0
	s_sub_i32 s3, s3, s7
	v_lshl_add_u32 v116, s3, v215, v223
	global_load_dwordx4 v[116:119], v116, s[44:45]
	v_mad_u32_u24 v120, s3, v199, v202
	global_load_dwordx2 v[120:121], v120, s[44:45]
	s_add_i32 s2, s23, s1
	s_add_i32 s3, s2, 3
	s_add_i32 s2, s2, 1
	s_cmp_ge_u32 s2, s34
	s_cselect_b32 s7, s34, 0
	s_sub_i32 s2, s2, s7
	s_cmp_ge_u32 s3, s34
	s_cselect_b32 s7, s34, 0
	s_sub_i32 s3, s3, s7
	s_cmp_ge_u32 s3, s34
	s_cselect_b32 s7, s34, 0
	s_sub_i32 s3, s3, s7
	v_lshl_add_u32 v122, s3, v215, v223
	global_load_dwordx4 v[122:125], v122, s[44:45]
	v_mad_u32_u24 v126, s3, v199, v202
	global_load_dwordx2 v[126:127], v126, s[44:45]
	v_lshl_add_u32 v128, s2, 7, v204
	global_load_dwordx4 v[128:131], v128, s[44:45]
	s_add_i32 s2, s23, s1
	s_add_i32 s3, s2, 4
	s_add_i32 s2, s2, 2
	s_cmp_ge_u32 s2, s34
	s_cselect_b32 s7, s34, 0
	s_sub_i32 s2, s2, s7
	s_cmp_ge_u32 s3, s34
	s_cselect_b32 s7, s34, 0
	s_sub_i32 s3, s3, s7
	s_cmp_ge_u32 s3, s34
	s_cselect_b32 s7, s34, 0
	s_sub_i32 s3, s3, s7
	v_lshl_add_u32 v156, s3, v215, v223
	global_load_dwordx4 v[156:159], v156, s[44:45]
	v_mad_u32_u24 v160, s3, v199, v202
	global_load_dwordx2 v[160:161], v160, s[44:45]
	v_lshl_add_u32 v162, s2, 7, v204
	global_load_dwordx4 v[162:165], v162, s[44:45]
	s_add_i32 s2, s23, s1
	s_add_i32 s3, s2, 5
	s_add_i32 s2, s2, 3
	s_cmp_ge_u32 s2, s34
	s_cselect_b32 s7, s34, 0
	s_sub_i32 s2, s2, s7
	s_cmp_ge_u32 s3, s34
	s_cselect_b32 s7, s34, 0
	s_sub_i32 s3, s3, s7
	s_cmp_ge_u32 s3, s34
	s_cselect_b32 s7, s34, 0
	s_sub_i32 s3, s3, s7
	s_mov_b32 s12, s3
	s_mov_b32 s13, s2
	s_waitcnt lgkmcnt(4)
	v_mfma_f32_32x32x16_bf16 v[84:99], v[166:169], v[132:135], 0
	ds_read_b128 v[166:169], v205 offset:20032
	v_exp_f32_e32 v20, v20
	v_exp_f32_e32 v4, v4
	v_exp_f32_e32 v21, v21
	v_add_f32_e32 v179, v4, v20
	v_exp_f32_e32 v5, v5
	s_waitcnt lgkmcnt(4)
	v_mfma_f32_32x32x16_bf16 v[68:83], v[170:173], v[132:135], 0
	ds_read_b128 v[170:173], v205 offset:13408
	s_waitcnt vmcnt(6)
	ds_write_b128 v219, v[116:119] offset:45056
	v_add_f32_e32 v179, v21, v179
	v_cvt_pk_bf16_f32 v100, v20, v21
	v_exp_f32_e32 v22, v22
	v_add_f32_e32 v179, v5, v179
	v_exp_f32_e32 v6, v6
	v_add_f32_e32 v179, v22, v179
	v_cvt_pk_bf16_f32 v108, v4, v5
	s_waitcnt lgkmcnt(5)
	v_mfma_f32_32x32x16_bf16 v[84:99], v[174:177], v[136:139], v[84:99]
	ds_read_b128 v[174:177], v205 offset:20064
	ds_write_b64 v220, v[120:121] offset:45056
	v_exp_f32_e32 v23, v23
	v_add_f32_e32 v179, v6, v179
	v_exp_f32_e32 v7, v7
	v_add_f32_e32 v179, v23, v179
	v_cvt_pk_bf16_f32 v101, v22, v23
	v_exp_f32_e32 v24, v24
	v_add_f32_e32 v179, v7, v179
	s_waitcnt lgkmcnt(6)
	v_mfma_f32_32x32x16_bf16 v[68:83], v[206:209], v[136:139], v[68:83]
	ds_read_b128 v[206:209], v205 offset:13440
	s_waitcnt vmcnt(4)
	ds_write_b128 v219, v[122:125] offset:58368
	v_exp_f32_e32 v8, v8
	v_add_f32_e32 v179, v24, v179
	v_cvt_pk_bf16_f32 v109, v6, v7
	v_exp_f32_e32 v25, v25
	v_add_f32_e32 v179, v8, v179
	v_exp_f32_e32 v9, v9
	s_waitcnt lgkmcnt(7)
	v_mfma_f32_32x32x16_bf16 v[84:99], v[226:229], v[140:143], v[84:99]
	ds_read_b128 v[226:229], v205 offset:20096
	ds_write_b64 v220, v[126:127] offset:58368
	v_add_f32_e32 v179, v25, v179
	v_cvt_pk_bf16_f32 v102, v24, v25
	v_exp_f32_e32 v26, v26
	v_add_f32_e32 v179, v9, v179
	v_exp_f32_e32 v10, v10
	v_add_f32_e32 v179, v26, v179
	v_cvt_pk_bf16_f32 v110, v8, v9
	s_waitcnt lgkmcnt(8)
	v_mfma_f32_32x32x16_bf16 v[68:83], v[166:169], v[140:143], v[68:83]
	ds_read_b128 v[166:169], v205 offset:13472
	s_waitcnt vmcnt(3)
	ds_write_b64 v221, v[128:129] offset:35840
	v_exp_f32_e32 v27, v27
	v_add_f32_e32 v179, v10, v179
	v_exp_f32_e32 v11, v11
	v_add_f32_e32 v179, v27, v179
	v_cvt_pk_bf16_f32 v103, v26, v27
	v_exp_f32_e32 v28, v28
	v_add_f32_e32 v179, v11, v179
	s_waitcnt lgkmcnt(9)
	v_mfma_f32_32x32x16_bf16 v[84:99], v[170:173], v[144:147], v[84:99]
	ds_read_b128 v[170:173], v205 offset:20128
	ds_write_b64 v222, v[130:131] offset:35840
	v_exp_f32_e32 v29, v29
	v_add_f32_e32 v179, v28, v179
	v_cvt_pk_bf16_f32 v111, v10, v11
	v_exp_f32_e32 v30, v30
	v_add_f32_e32 v179, v29, v179
	v_exp_f32_e32 v31, v31
	s_waitcnt lgkmcnt(9)
	v_mfma_f32_32x32x16_bf16 v[68:83], v[174:177], v[144:147], v[68:83]
	s_waitcnt vmcnt(1)
	ds_write_b128 v232, v[156:159] offset:6144
	v_add_f32_e32 v179, v30, v179
	v_cvt_pk_bf16_f32 v104, v28, v29
	v_exp_f32_e32 v32, v32
	v_add_f32_e32 v179, v31, v179
	v_exp_f32_e32 v33, v33
	v_add_f32_e32 v179, v32, v179
	v_cvt_pk_bf16_f32 v105, v30, v31
	s_waitcnt lgkmcnt(8)
	v_mfma_f32_32x32x16_bf16 v[84:99], v[206:209], v[148:151], v[84:99]
	ds_write_b64 v233, v[160:161] offset:6144
	v_exp_f32_e32 v34, v34
	v_add_f32_e32 v179, v33, v179
	v_exp_f32_e32 v35, v35
	v_add_f32_e32 v179, v34, v179
	v_cvt_pk_bf16_f32 v106, v32, v33
	v_exp_f32_e32 v12, v12
	v_add_f32_e32 v179, v35, v179
	s_waitcnt lgkmcnt(7)
	v_mfma_f32_32x32x16_bf16 v[68:83], v[226:229], v[148:151], v[68:83]
	s_waitcnt vmcnt(0)
	ds_write_b64 v234, v[162:163] offset:19456
	v_exp_f32_e32 v13, v13
	v_add_f32_e32 v179, v12, v179
	v_cvt_pk_bf16_f32 v107, v34, v35
	v_exp_f32_e32 v14, v14
	v_add_f32_e32 v179, v13, v179
	v_exp_f32_e32 v15, v15
	s_waitcnt lgkmcnt(6)
	v_mfma_f32_32x32x16_bf16 v[84:99], v[166:169], v[152:155], v[84:99]
	ds_write_b64 v235, v[164:165] offset:19456
	v_add_f32_e32 v179, v14, v179
	v_cvt_pk_bf16_f32 v112, v12, v13
	v_exp_f32_e32 v16, v16
	v_add_f32_e32 v179, v15, v179
	v_exp_f32_e32 v17, v17
	v_add_f32_e32 v179, v16, v179
	v_cvt_pk_bf16_f32 v113, v14, v15
	s_waitcnt lgkmcnt(5)
	v_mfma_f32_32x32x16_bf16 v[68:83], v[170:173], v[152:155], v[68:83]
	v_lshl_add_u32 v156, s12, v215, v223
	global_load_dwordx4 v[156:159], v156, s[44:45]
	v_mad_u32_u24 v160, s12, v199, v202
	global_load_dwordx2 v[160:161], v160, s[44:45]
	v_lshl_add_u32 v162, s13, 7, v204
	global_load_dwordx4 v[162:165], v162, s[44:45]
	s_add_i32 s12, s12, 1
	s_cmp_eq_u32 s12, s34
	s_cselect_b32 s12, 0, s12
	s_add_i32 s13, s13, 1
	s_cmp_eq_u32 s13, s34
	s_cselect_b32 s13, 0, s13
	v_exp_f32_e32 v18, v18
	v_add_f32_e32 v179, v17, v179
	v_exp_f32_e32 v19, v19
	v_add_f32_e32 v179, v18, v179
	v_cvt_pk_bf16_f32 v114, v16, v17
	v_add_f32_e32 v179, v19, v179
	v_cvt_pk_bf16_f32 v115, v18, v19
	v_add_f32_e32 v224, v224, v179
	s_add_i32 s1, s1, 1
	s_waitcnt lgkmcnt(0)
	s_barrier
	ds_read_b128 v[166:169], v205 offset:45056
	ds_read_b128 v[170:173], v205 offset:51712
	ds_read_b128 v[174:177], v205 offset:45088
	ds_read_b128 v[206:209], v205 offset:51744
	ds_read_b128 v[226:229], v205 offset:45120
	s_waitcnt lgkmcnt(0)
	s_nop 0
